# post1/post2: transposed-value blocks dealt to the waves that do not already have an extra row trip
# baseline (speedup 1.0000x reference)
.LBB0_474:
	s_or_b64 exec, exec, s[46:47]
	v_mov_b32_e32 v2, s40
	v_lshl_add_u32 v37, s41, 12, v2
	s_movk_i32 s2, 0x210
	v_lshrrev_b32_e32 v2, 1, v51
	v_lshlrev_b32_e32 v3, 6, v67
	v_mov_b32_e32 v36, v50
	s_cmp_eq_u32 s39, 0x800
	s_cbranch_scc0 .Lvt_a
	v_sub_u32_e32 v36, 0x7ff, v50
.Lvt_a:
	v_cmp_gt_i32_e32 vcc, s2, v36
	v_mul_hi_u32_u24_e32 v31, 0x2e00, v67
	v_mul_u32_u24_e32 v30, 0x2e00, v67
	v_and_b32_e32 v41, 3, v51
	v_mul_hi_u32_u24_e32 v33, 0x2100, v67
	v_mul_u32_u24_e32 v32, 0x2100, v67
	v_and_b32_e32 v42, 32, v56
	v_and_b32_e32 v43, 28, v2
	v_add_u32_e32 v40, v37, v3
	s_and_saveexec_b64 s[2:3], vcc
	v_readlane_b32 s88, v255, 26
	s_movk_i32 s40, 0x83f
	v_readlane_b32 s89, v255, 27
	v_readlane_b32 s90, v255, 28
	v_readlane_b32 s91, v255, 29
	s_cbranch_execz .LBB0_477
	s_mov_b64 s[4:5], 0x70000000
	v_or3_b32 v2, v43, v41, v42
	v_lshl_add_u64 v[34:35], v[54:55], 0, s[4:5]
	v_add_u32_e32 v44, v37, v2
	s_mov_b64 s[4:5], 0

.LBB0_477:
	s_or_b64 exec, exec, s[2:3]
	s_cmp_eq_u32 s39, 0x800
	s_cbranch_scc0 .Lvt_c
	v_xor_b32_e32 v50, 0x400, v50
.Lvt_c:
	s_movk_i32 s2, 0x840
	s_mov_b64 s[60:61], 0x10000
	s_mov_b32 s81, s38
	v_cmp_gt_i32_e32 vcc, s2, v50
	s_and_saveexec_b64 s[2:3], vcc
	v_readlane_b32 s62, v255, 33
	s_mov_b64 s[56:57], 0x20000
	s_mov_b32 s63, s33
	s_mov_b32 s80, s36
	s_cbranch_execz .LBB0_480
	s_mov_b64 s[4:5], 0x74200000
	v_or3_b32 v2, v43, v41, v42
	v_lshl_add_u64 v[34:35], v[54:55], 0, s[4:5]
	v_add_u32_e32 v38, v37, v2
	s_mov_b64 s[4:5], 0

.LBB0_617:
	s_or_b64 exec, exec, s[2:3]
	s_cmp_eq_u32 s16, 0x800
	s_cbranch_scc0 .Lvt_b
	v_xor_b32_e32 v38, 0x400, v38
.Lvt_b:
	s_movk_i32 s2, 0x840
	v_mov_b32_e32 v2, s18
	v_cmp_gt_i32_e32 vcc, s2, v38
	s_and_saveexec_b64 s[2:3], vcc
	s_cbranch_execz .LBB0_620
	v_lshlrev_b32_e32 v3, 3, v47
	v_lshrrev_b32_e32 v4, 1, v39
	v_and_b32_e32 v3, 32, v3
	v_and_b32_e32 v4, 28, v4
	v_lshl_add_u32 v2, s17, 12, v2
	v_or3_b32 v3, v4, v3, v49
	s_mov_b64 s[4:5], 0x72500000
	v_add_u32_e32 v39, v2, v3
	v_lshlrev_b32_e32 v3, 6, v47
	v_lshl_add_u64 v[30:31], v[42:43], 0, s[4:5]
	v_mul_hi_u32_u24_e32 v33, 0xe00, v47
	v_mul_u32_u24_e32 v32, 0xe00, v47
	v_mul_hi_u32_u24_e32 v35, 0x2100, v47
	v_mul_u32_u24_e32 v34, 0x2100, v47
	s_mov_b64 s[4:5], 0
	v_add_u32_e32 v42, v2, v3
